# MoE hand-off: early readiness read before the epilogue, and no full memory drain after the acquire invalidate (the K-loop's counted waits and barriers cover it)
# speedup vs baseline: 1.0014x; 1.0014x over previous
.LBB0_2052:
	s_waitcnt lgkmcnt(0)
	buffer_inv sc1
.LBB0_2053:
	s_barrier
